# w_in GEMM gate-tile epilogue: the seven per-row scale loads issued together at entry; per-row-block full drains (store, store, load, wait) removed
# baseline (speedup 1.0000x reference)
;     __device__ __forceinline__ void operator()(const f32x4 (&acc)[2][2][4][2], const Unit& u, int wr, int wc, int fr, int fq) const {
;     ...
;             if (wc == 0 && fq < 2) { float* g = (float*)u.O; const f32x4 b0 = *(const f32x4*)(bif + 8 * fq), b1 = *(const f32x4*)(bif + 8 * fq + 4); const f32x4 s0 = *(const f32x4*)(sB + 8 * fq), s1 = *(const f32x4*)(sB + 8 * fq + 4);
; #pragma unroll
;                 for (int ai = 0; ai < 2; ++ai)
; #pragma unroll
;                     for (int m = 0; m < 4; ++m) { const int r = row0 + ai * HALF + m * 16; const float sr = sA[r]; float* rp = g + (size_t)r * 16 + 8 * fq;
;                         const i32x4_t a0 = __builtin_bit_cast(i32x4_t, acc[ai][0][m][0]), a1 = __builtin_bit_cast(i32x4_t, acc[ai][0][m][1]);
;                         *(f32x4*)rp = __builtin_convertvector(a0, f32x4) * sr * s0 + b0; *(f32x4*)(rp + 4) = __builtin_convertvector(a1, f32x4) * sr * s1 + b1; } }
.LBB0_350:
	v_cmp_gt_i32_e32 vcc, 2, v147
	s_and_b64 s[2:3], s[14:15], vcc
	s_and_saveexec_b64 s[54:55], s[2:3]
	s_cbranch_execz .LBB0_352
	v_ashrrev_i32_e32 v145, 31, v144
	v_ashrrev_i32_e32 v147, 31, v146
	v_lshl_add_u64 v[80:81], v[144:145], 2, s[50:51]
	v_lshlrev_b64 v[82:83], 2, v[146:147]
	global_load_dword v84, v[80:81], off
	global_load_dword v120, v[80:81], off offset:64
	global_load_dword v121, v[80:81], off offset:128
	global_load_dword v122, v[80:81], off offset:192
	global_load_dword v123, v[80:81], off offset:512
	global_load_dword v124, v[80:81], off offset:576
	global_load_dword v125, v[80:81], off offset:640
	global_load_dword v126, v[80:81], off offset:704
	s_waitcnt vmcnt(12)
	v_lshl_add_u64 v[64:65], s[16:17], 0, v[82:83]
	s_waitcnt vmcnt(9)
	v_lshl_add_u64 v[76:77], s[52:53], 0, v[82:83]
	global_load_dwordx4 v[68:71], v[76:77], off
	global_load_dwordx4 v[72:75], v[64:65], off
	s_nop 0
	global_load_dwordx4 v[64:67], v[64:65], off offset:16
	s_nop 0
	global_load_dwordx4 v[76:79], v[76:77], off offset:16
	v_cvt_f32_i32_e32 v63, v63
	v_cvt_f32_i32_e32 v62, v62
	v_cvt_f32_i32_e32 v61, v61
	v_cvt_f32_i32_e32 v60, v60
	v_cvt_f32_i32_e32 v59, v59
	v_cvt_f32_i32_e32 v58, v58
	v_cvt_f32_i32_e32 v87, v57
	v_cvt_f32_i32_e32 v86, v56
	v_lshlrev_b64 v[56:57], 6, v[144:145]
	v_lshl_add_u64 v[88:89], s[44:45], 0, v[82:83]
	v_lshl_add_u64 v[56:57], v[88:89], 0, v[56:57]
	v_cvt_f32_i32_e32 v55, v55
	v_cvt_f32_i32_e32 v54, v54
	v_cvt_f32_i32_e32 v53, v53
	v_cvt_f32_i32_e32 v52, v52
	v_cvt_f32_i32_e32 v51, v51
	v_cvt_f32_i32_e32 v50, v50
	v_cvt_f32_i32_e32 v49, v49
	v_cvt_f32_i32_e32 v48, v48
	v_cvt_f32_i32_e32 v47, v47
	v_cvt_f32_i32_e32 v46, v46
	v_cvt_f32_i32_e32 v45, v45
	v_cvt_f32_i32_e32 v44, v44
	v_cvt_f32_i32_e32 v43, v43
	v_cvt_f32_i32_e32 v42, v42
	v_cvt_f32_i32_e32 v41, v41
	v_cvt_f32_i32_e32 v40, v40
	v_cvt_f32_i32_e32 v39, v39
	v_cvt_f32_i32_e32 v38, v38
	v_cvt_f32_i32_e32 v37, v37
	v_cvt_f32_i32_e32 v36, v36
	v_cvt_f32_i32_e32 v35, v35
	v_cvt_f32_i32_e32 v34, v34
	v_cvt_f32_i32_e32 v33, v33
	v_cvt_f32_i32_e32 v32, v32
	v_cvt_f32_i32_e32 v31, v31
	v_cvt_f32_i32_e32 v30, v30
	v_cvt_f32_i32_e32 v29, v29
	v_cvt_f32_i32_e32 v28, v28
	v_cvt_f32_i32_e32 v27, v27
	v_cvt_f32_i32_e32 v26, v26
	v_cvt_f32_i32_e32 v25, v25
	v_cvt_f32_i32_e32 v24, v24
	s_mov_b64 s[2:3], 0x2000
	v_cvt_f32_i32_e32 v23, v23
	v_cvt_f32_i32_e32 v22, v22
	v_cvt_f32_i32_e32 v21, v21
	v_cvt_f32_i32_e32 v20, v20
	v_cvt_f32_i32_e32 v19, v19
	v_cvt_f32_i32_e32 v18, v18
	v_cvt_f32_i32_e32 v17, v17
	v_cvt_f32_i32_e32 v16, v16
	v_cvt_f32_i32_e32 v15, v15
	v_cvt_f32_i32_e32 v14, v14
	v_cvt_f32_i32_e32 v13, v13
	v_cvt_f32_i32_e32 v12, v12
	v_cvt_f32_i32_e32 v11, v11
	v_cvt_f32_i32_e32 v10, v10
	v_cvt_f32_i32_e32 v9, v9
	v_cvt_f32_i32_e32 v8, v8
	v_cvt_f32_i32_e32 v7, v7
	v_cvt_f32_i32_e32 v6, v6
	v_cvt_f32_i32_e32 v5, v5
	v_cvt_f32_i32_e32 v4, v4
	v_cvt_f32_i32_e32 v3, v3
	v_cvt_f32_i32_e32 v2, v2
	v_cvt_f32_i32_e32 v1, v1
	v_cvt_f32_i32_e32 v0, v0
	s_waitcnt vmcnt(4)
	v_pk_mul_f32 v[82:83], v[84:85], v[60:61] op_sel_hi:[0,1]
	v_pk_mul_f32 v[60:61], v[84:85], v[62:63] op_sel_hi:[0,1]
	v_pk_mul_f32 v[62:63], v[84:85], v[86:87] op_sel_hi:[0,1]
	v_pk_mul_f32 v[84:85], v[84:85], v[58:59] op_sel_hi:[0,1]
	s_waitcnt vmcnt(2)
	v_pk_fma_f32 v[60:61], v[70:71], v[60:61], v[74:75]
	v_pk_fma_f32 v[58:59], v[68:69], v[82:83], v[72:73]
	s_waitcnt vmcnt(0)
;     __device__ __forceinline__ void operator()(const f32x4 (&acc)[2][2][4][2], const Unit& u, int wr, int wc, int fr, int fq) const {
;     ...
;             if (wc == 0 && fq < 2) { float* g = (float*)u.O; const f32x4 b0 = *(const f32x4*)(bif + 8 * fq), b1 = *(const f32x4*)(bif + 8 * fq + 4); const f32x4 s0 = *(const f32x4*)(sB + 8 * fq), s1 = *(const f32x4*)(sB + 8 * fq + 4);
; #pragma unroll
;                 for (int ai = 0; ai < 2; ++ai)
; #pragma unroll
;                     for (int m = 0; m < 4; ++m) { const int r = row0 + ai * HALF + m * 16; const float sr = sA[r]; float* rp = g + (size_t)r * 16 + 8 * fq;
;                         const i32x4_t a0 = __builtin_bit_cast(i32x4_t, acc[ai][0][m][0]), a1 = __builtin_bit_cast(i32x4_t, acc[ai][0][m][1]);
;                         *(f32x4*)rp = __builtin_convertvector(a0, f32x4) * sr * s0 + b0; *(f32x4*)(rp + 4) = __builtin_convertvector(a1, f32x4) * sr * s1 + b1; } }
	v_pk_fma_f32 v[84:85], v[78:79], v[84:85], v[66:67]
	v_pk_fma_f32 v[82:83], v[76:77], v[62:63], v[64:65]
	global_store_dwordx4 v[56:57], v[58:61], off
	global_store_dwordx4 v[56:57], v[82:85], off offset:16
	s_nop 0
	v_mov_b32_e32 v58, v120
	v_or_b32_e32 v60, 16, v144
	v_ashrrev_i32_e32 v61, 31, v60
	v_lshlrev_b64 v[60:61], 6, v[60:61]
	v_lshl_add_u64 v[60:61], v[88:89], 0, v[60:61]
	v_pk_mul_f32 v[52:53], v[58:59], v[52:53] op_sel_hi:[0,1]
	v_pk_mul_f32 v[54:55], v[58:59], v[54:55] op_sel_hi:[0,1]
	v_pk_mul_f32 v[62:63], v[58:59], v[48:49] op_sel_hi:[0,1]
	v_pk_mul_f32 v[58:59], v[58:59], v[50:51] op_sel_hi:[0,1]
	v_pk_fma_f32 v[50:51], v[70:71], v[54:55], v[74:75]
	v_pk_fma_f32 v[48:49], v[68:69], v[52:53], v[72:73]
	v_pk_fma_f32 v[54:55], v[78:79], v[58:59], v[66:67]
	v_pk_fma_f32 v[52:53], v[76:77], v[62:63], v[64:65]
	global_store_dwordx4 v[60:61], v[48:51], off
	global_store_dwordx4 v[60:61], v[52:55], off offset:16
	s_nop 0
	v_mov_b32_e32 v48, v121
	v_or_b32_e32 v50, 32, v144
	v_ashrrev_i32_e32 v51, 31, v50
	v_lshlrev_b64 v[50:51], 6, v[50:51]
	v_lshl_add_u64 v[50:51], v[88:89], 0, v[50:51]
	v_pk_mul_f32 v[44:45], v[48:49], v[44:45] op_sel_hi:[0,1]
	v_pk_mul_f32 v[46:47], v[48:49], v[46:47] op_sel_hi:[0,1]
	v_pk_mul_f32 v[52:53], v[48:49], v[40:41] op_sel_hi:[0,1]
	v_pk_mul_f32 v[48:49], v[48:49], v[42:43] op_sel_hi:[0,1]
	v_pk_fma_f32 v[42:43], v[70:71], v[46:47], v[74:75]
	v_pk_fma_f32 v[40:41], v[68:69], v[44:45], v[72:73]
	v_pk_fma_f32 v[46:47], v[78:79], v[48:49], v[66:67]
	v_pk_fma_f32 v[44:45], v[76:77], v[52:53], v[64:65]
	global_store_dwordx4 v[50:51], v[40:43], off
	global_store_dwordx4 v[50:51], v[44:47], off offset:16
	s_nop 0
	v_mov_b32_e32 v40, v122
	v_or_b32_e32 v42, 48, v144
	v_ashrrev_i32_e32 v43, 31, v42
	v_lshlrev_b64 v[42:43], 6, v[42:43]
	v_lshl_add_u64 v[42:43], v[88:89], 0, v[42:43]
	v_pk_mul_f32 v[36:37], v[40:41], v[36:37] op_sel_hi:[0,1]
	v_pk_mul_f32 v[38:39], v[40:41], v[38:39] op_sel_hi:[0,1]
	v_pk_mul_f32 v[44:45], v[40:41], v[32:33] op_sel_hi:[0,1]
	v_pk_mul_f32 v[40:41], v[40:41], v[34:35] op_sel_hi:[0,1]
	v_pk_fma_f32 v[34:35], v[70:71], v[38:39], v[74:75]
	v_pk_fma_f32 v[32:33], v[68:69], v[36:37], v[72:73]
	v_pk_fma_f32 v[38:39], v[78:79], v[40:41], v[66:67]
	v_pk_fma_f32 v[36:37], v[76:77], v[44:45], v[64:65]
	global_store_dwordx4 v[42:43], v[32:35], off
	global_store_dwordx4 v[42:43], v[36:39], off offset:16
	s_nop 0
	v_mov_b32_e32 v32, v123
	v_lshl_add_u64 v[34:35], v[56:57], 0, s[2:3]
	s_movk_i32 s2, 0x2000
	v_add_co_u32_e32 v36, vcc, s2, v56
	s_mov_b64 s[2:3], 0x2400
	s_nop 0
	v_addc_co_u32_e32 v37, vcc, 0, v57, vcc
	v_pk_mul_f32 v[28:29], v[32:33], v[28:29] op_sel_hi:[0,1]
	v_pk_mul_f32 v[30:31], v[32:33], v[30:31] op_sel_hi:[0,1]
	v_pk_mul_f32 v[38:39], v[32:33], v[24:25] op_sel_hi:[0,1]
	v_pk_mul_f32 v[32:33], v[32:33], v[26:27] op_sel_hi:[0,1]
	v_pk_fma_f32 v[26:27], v[70:71], v[30:31], v[74:75]
	v_pk_fma_f32 v[24:25], v[68:69], v[28:29], v[72:73]
	v_pk_fma_f32 v[30:31], v[78:79], v[32:33], v[66:67]
	v_pk_fma_f32 v[28:29], v[76:77], v[38:39], v[64:65]
	global_store_dwordx4 v[36:37], v[24:27], off
	global_store_dwordx4 v[34:35], v[28:31], off offset:16
	s_nop 0
	v_mov_b32_e32 v24, v124
	v_lshl_add_u64 v[26:27], v[56:57], 0, s[2:3]
	v_pk_mul_f32 v[20:21], v[24:25], v[20:21] op_sel_hi:[0,1]
	v_pk_mul_f32 v[22:23], v[24:25], v[22:23] op_sel_hi:[0,1]
	v_pk_mul_f32 v[28:29], v[24:25], v[16:17] op_sel_hi:[0,1]
	v_pk_mul_f32 v[24:25], v[24:25], v[18:19] op_sel_hi:[0,1]
	v_pk_fma_f32 v[18:19], v[70:71], v[22:23], v[74:75]
	v_pk_fma_f32 v[16:17], v[68:69], v[20:21], v[72:73]
	v_pk_fma_f32 v[22:23], v[78:79], v[24:25], v[66:67]
	v_pk_fma_f32 v[20:21], v[76:77], v[28:29], v[64:65]
	global_store_dwordx4 v[36:37], v[16:19], off offset:1024
	global_store_dwordx4 v[26:27], v[20:23], off offset:16
	s_nop 0
	v_mov_b32_e32 v16, v125
	v_lshl_add_u64 v[18:19], v[56:57], 0, s[22:23]
	v_pk_mul_f32 v[12:13], v[16:17], v[12:13] op_sel_hi:[0,1]
	v_pk_mul_f32 v[14:15], v[16:17], v[14:15] op_sel_hi:[0,1]
	v_pk_mul_f32 v[20:21], v[16:17], v[8:9] op_sel_hi:[0,1]
	v_pk_mul_f32 v[16:17], v[16:17], v[10:11] op_sel_hi:[0,1]
	v_pk_fma_f32 v[10:11], v[70:71], v[14:15], v[74:75]
	v_pk_fma_f32 v[8:9], v[68:69], v[12:13], v[72:73]
	v_pk_fma_f32 v[14:15], v[78:79], v[16:17], v[66:67]
	v_pk_fma_f32 v[12:13], v[76:77], v[20:21], v[64:65]
	global_store_dwordx4 v[36:37], v[8:11], off offset:2048
	global_store_dwordx4 v[18:19], v[12:15], off offset:16
	s_nop 0
	v_mov_b32_e32 v8, v126
	v_lshl_add_u64 v[10:11], v[56:57], 0, s[38:39]
	v_pk_mul_f32 v[4:5], v[8:9], v[4:5] op_sel_hi:[0,1]
	v_pk_mul_f32 v[6:7], v[8:9], v[6:7] op_sel_hi:[0,1]
	v_pk_mul_f32 v[12:13], v[8:9], v[0:1] op_sel_hi:[0,1]
	v_pk_mul_f32 v[8:9], v[8:9], v[2:3] op_sel_hi:[0,1]
	v_pk_fma_f32 v[2:3], v[70:71], v[6:7], v[74:75]
	v_pk_fma_f32 v[0:1], v[68:69], v[4:5], v[72:73]
	v_pk_fma_f32 v[6:7], v[78:79], v[8:9], v[66:67]
	v_pk_fma_f32 v[4:5], v[76:77], v[12:13], v[64:65]
	global_store_dwordx4 v[36:37], v[0:3], off offset:3072
	global_store_dwordx4 v[10:11], v[4:7], off offset:16
